# P2: counted waits for the next sub-block's Q prefetch account for the LSE store of dilated-group units (vmcnt 4/3 instead of 3/2), on top of the scalar sink load
# speedup vs baseline: 1.0131x; 1.0048x over previous
.LBB0_342:
	s_cmp_lg_u64 s[96:97], 0
	s_cbranch_scc1 .Lq1_lse
	s_waitcnt vmcnt(3)
	s_branch .Lq1_done

.Lq1_done:
	v_cvt_pk_f32_fp8_sdwa v[4:5], v154 src0_sel:WORD_1
	v_cvt_pk_f32_fp8_e32 v[6:7], v154
	v_cvt_pk_f32_fp8_sdwa v[8:9], v155 src0_sel:WORD_1
	v_cvt_pk_f32_fp8_e32 v[10:11], v155
	v_pk_mul_f32 v[4:5], v[4:5], s[34:35] op_sel_hi:[1,0]
	v_pk_mul_f32 v[6:7], v[6:7], s[34:35] op_sel_hi:[1,0]
	v_pk_mul_f32 v[8:9], v[8:9], s[34:35] op_sel_hi:[1,0]
	v_pk_mul_f32 v[10:11], v[10:11], s[34:35] op_sel_hi:[1,0]
	v_cvt_pk_bf16_f32 v138, v6, v7
	v_cvt_pk_bf16_f32 v139, v4, v5
	v_cvt_pk_bf16_f32 v140, v10, v11
	v_cvt_pk_bf16_f32 v141, v8, v9
	v_cvt_pk_f32_fp8_sdwa v[4:5], v156 src0_sel:WORD_1
	v_cvt_pk_f32_fp8_e32 v[6:7], v156
	v_cvt_pk_f32_fp8_sdwa v[8:9], v157 src0_sel:WORD_1
	v_cvt_pk_f32_fp8_e32 v[10:11], v157
	v_pk_mul_f32 v[4:5], v[4:5], s[34:35] op_sel_hi:[1,0]
	v_pk_mul_f32 v[6:7], v[6:7], s[34:35] op_sel_hi:[1,0]
	v_pk_mul_f32 v[8:9], v[8:9], s[34:35] op_sel_hi:[1,0]
	v_pk_mul_f32 v[10:11], v[10:11], s[34:35] op_sel_hi:[1,0]
	v_cvt_pk_bf16_f32 v142, v6, v7
	v_cvt_pk_bf16_f32 v143, v4, v5
	v_cvt_pk_bf16_f32 v144, v10, v11
	v_cvt_pk_bf16_f32 v145, v8, v9
	s_cmp_lg_u64 s[96:97], 0
	s_cbranch_scc1 .Lq2_lse
	s_waitcnt vmcnt(2)
	s_branch .Lq2_done

.Lq2_done:
	v_cvt_pk_f32_fp8_sdwa v[4:5], v158 src0_sel:WORD_1
	v_cvt_pk_f32_fp8_e32 v[6:7], v158
	v_cvt_pk_f32_fp8_sdwa v[8:9], v159 src0_sel:WORD_1
	v_cvt_pk_f32_fp8_e32 v[10:11], v159
	v_pk_mul_f32 v[4:5], v[4:5], s[34:35] op_sel_hi:[1,0]
	v_pk_mul_f32 v[6:7], v[6:7], s[34:35] op_sel_hi:[1,0]
	v_pk_mul_f32 v[8:9], v[8:9], s[34:35] op_sel_hi:[1,0]
	v_pk_mul_f32 v[10:11], v[10:11], s[34:35] op_sel_hi:[1,0]
	v_cvt_pk_bf16_f32 v146, v6, v7
	v_cvt_pk_bf16_f32 v147, v4, v5
	v_cvt_pk_bf16_f32 v148, v10, v11
	v_cvt_pk_bf16_f32 v149, v8, v9
	v_cvt_pk_f32_fp8_sdwa v[4:5], v160 src0_sel:WORD_1
	v_cvt_pk_f32_fp8_e32 v[6:7], v160
	v_cvt_pk_f32_fp8_sdwa v[8:9], v161 src0_sel:WORD_1
	v_cvt_pk_f32_fp8_e32 v[10:11], v161
	v_pk_mul_f32 v[4:5], v[4:5], s[34:35] op_sel_hi:[1,0]
	v_pk_mul_f32 v[6:7], v[6:7], s[34:35] op_sel_hi:[1,0]
	v_pk_mul_f32 v[8:9], v[8:9], s[34:35] op_sel_hi:[1,0]
	v_pk_mul_f32 v[10:11], v[10:11], s[34:35] op_sel_hi:[1,0]
	v_cvt_pk_bf16_f32 v150, v6, v7
	v_cvt_pk_bf16_f32 v151, v4, v5
	v_cvt_pk_bf16_f32 v152, v10, v11
	v_cvt_pk_bf16_f32 v153, v8, v9
	s_and_b64 vcc, exec, s[40:41]
	s_cbranch_vccnz .LBB0_344
